# grouped GEMM epilogue: column-scale quads loaded and scaled once per unit instead of per half-round (16 drains removed)
# speedup vs baseline: 1.0137x; 1.0014x over previous
; #define GAS __attribute__((address_space(1)))
; #define LAS __attribute__((address_space(3)))
;     __device__ __forceinline__ void operator()(const f32x4 (&acc)[2][2][4][2], const Unit& u, const float (&rs)[2][4], int wr, int wc, int fr, int fq) const {
;         const int colw = u.pn * BM + wc * 64;
;         const int L = fr + 16 * fq, rr = L >> 2, sg = L & 3;
;         LAS unsigned char* wp0 = tb + fr * 64 + ((fq) ^ (fr & 7)) * 8; LAS unsigned char* wp1 = tb + fr * 64 + ((4 + fq) ^ (fr & 7)) * 8;
;         const LAS unsigned char* rp0 = tb + rr * 64 + ((2 * sg) ^ (rr & 7)) * 8; const LAS unsigned char* rp1 = tb + rr * 64 + ((2 * sg + 1) ^ (rr & 7)) * 8;
;         unsigned char* gp = O + (size_t)(u.pm * BM + wr * 64 + rr) * ldc + colw + sg * 16;
;     ...
;         F8_PACKW(0);
; #pragma unroll
;         for (int st = 0; st < 8; ++st) {
;             asm volatile("" ::: "memory");
;             const u32x2_t a = *(const LAS u32x2_t*)(rp0 + (st & 1) * 1024), b = *(const LAS u32x2_t*)(rp1 + (st & 1) * 1024);
;             asm volatile("" ::: "memory");
;             if (st + 1 < 8) F8_PACKW(st + 1);
;             u32x4 o; o.x = a.x; o.y = a.y; o.z = b.x; o.w = b.y;
;             *(GAS u32x4*)(gp + (size_t)((st >> 2) * HALF + (st & 3) * 16) * ldc) = o; }
.LBB0_1033:
	s_lshl_b32 s40, s72, 8
	s_or_b32 s60, s40, s67
	s_ashr_i32 s61, s60, 31
	v_cndmask_b32_e64 v2, 0, 1, s[50:51]
	v_cmp_ne_u32_e64 s[40:41], 1, v2
	s_andn2_b64 vcc, exec, s[50:51]
	v_lshl_add_u64 v[144:145], s[60:61], 2, v[142:143]
	s_cbranch_vccnz .LBB0_1035
	global_load_dwordx4 v[234:237], v[144:145], off
	global_load_dwordx4 v[238:241], v[144:145], off offset:16
	global_load_dwordx4 v[242:245], v[144:145], off offset:128
	global_load_dwordx4 v[246:249], v[144:145], off offset:144
	s_waitcnt vmcnt(0)
	v_pk_mul_f32 v[234:235], v[234:235], s[58:59] op_sel_hi:[1,0]
	v_pk_mul_f32 v[236:237], v[236:237], s[58:59] op_sel_hi:[1,0]
	v_pk_mul_f32 v[238:239], v[238:239], s[58:59] op_sel_hi:[1,0]
	v_pk_mul_f32 v[240:241], v[240:241], s[58:59] op_sel_hi:[1,0]
	v_pk_mul_f32 v[242:243], v[242:243], s[58:59] op_sel_hi:[1,0]
	v_pk_mul_f32 v[244:245], v[244:245], s[58:59] op_sel_hi:[1,0]
	v_pk_mul_f32 v[246:247], v[246:247], s[58:59] op_sel_hi:[1,0]
	v_pk_mul_f32 v[248:249], v[248:249], s[58:59] op_sel_hi:[1,0]
	v_pk_mul_f32 v[130:131], v[130:131], v[236:237]
	v_pk_mul_f32 v[128:129], v[128:129], v[234:235]
	v_pk_mul_f32 v[126:127], v[126:127], v[240:241]
	v_pk_mul_f32 v[124:125], v[124:125], v[238:239]
.LBB0_1035:
	s_and_b64 vcc, exec, s[40:41]
	s_cbranch_vccnz .LBB0_1037
	v_pk_mul_f32 v[122:123], v[122:123], v[244:245]
	v_pk_mul_f32 v[120:121], v[120:121], v[242:243]
	v_pk_mul_f32 v[118:119], v[118:119], v[248:249]
	v_pk_mul_f32 v[116:117], v[116:117], v[246:247]
.LBB0_1037:
	v_mov_b32_e32 v152, v3
	v_mov_b32_e32 v153, v3
	v_cvt_pk_fp8_f32 v152, v128, v129
	v_cvt_pk_fp8_f32 v153, v124, v125
	v_mov_b32_e32 v124, v3
	v_mov_b32_e32 v125, v3
	v_cvt_pk_fp8_f32 v124, v120, v121
	v_cvt_pk_fp8_f32 v125, v116, v117
	v_cvt_pk_fp8_f32 v152, v130, v131 op_sel:[0,0,1]
	v_cvt_pk_fp8_f32 v153, v126, v127 op_sel:[0,0,1]
	v_cvt_pk_fp8_f32 v124, v122, v123 op_sel:[0,0,1]
	v_cvt_pk_fp8_f32 v125, v118, v119 op_sel:[0,0,1]
	ds_write_b64 v148, v[152:153]
	ds_write_b64 v149, v[124:125]
	ds_read_b64 v[116:117], v150
	ds_read_b64 v[118:119], v151
	s_and_b64 vcc, exec, s[40:41]
	s_cbranch_vccnz .LBB0_1039
	v_pk_mul_f32 v[114:115], v[114:115], v[236:237]
	v_pk_mul_f32 v[112:113], v[112:113], v[234:235]
	v_pk_mul_f32 v[110:111], v[110:111], v[240:241]
	v_pk_mul_f32 v[108:109], v[108:109], v[238:239]
.LBB0_1039:
	s_and_b64 vcc, exec, s[40:41]
	s_cbranch_vccnz .LBB0_1041
	v_pk_mul_f32 v[106:107], v[106:107], v[244:245]
	v_pk_mul_f32 v[104:105], v[104:105], v[242:243]
	v_pk_mul_f32 v[102:103], v[102:103], v[248:249]
	v_pk_mul_f32 v[100:101], v[100:101], v[246:247]
.LBB0_1041:
	v_mov_b32_e32 v121, v3
	v_cvt_pk_fp8_f32 v121, v108, v109
	v_mov_b32_e32 v120, v3
	v_cvt_pk_fp8_f32 v120, v112, v113
	v_lshl_add_u32 v108, s71, 8, v146
	v_cvt_pk_fp8_f32 v121, v110, v111 op_sel:[0,0,1]
	v_mov_b32_e32 v110, v3
	v_mov_b32_e32 v111, v3
	v_cvt_pk_fp8_f32 v110, v104, v105
	v_cvt_pk_fp8_f32 v111, v100, v101
	v_ashrrev_i32_e32 v109, 31, v108
	v_cvt_pk_fp8_f32 v120, v114, v115 op_sel:[0,0,1]
	v_lshlrev_b64 v[100:101], 10, v[108:109]
	v_lshl_add_u64 v[100:101], s[42:43], 0, v[100:101]
	v_cvt_pk_fp8_f32 v110, v106, v107 op_sel:[0,0,1]
	v_cvt_pk_fp8_f32 v111, v102, v103 op_sel:[0,0,1]
	v_lshl_add_u64 v[100:101], v[100:101], 0, s[60:61]
	v_lshl_add_u64 v[104:105], v[100:101], 0, v[140:141]
	ds_write_b64 v148, v[120:121] offset:1024
	ds_write_b64 v149, v[110:111] offset:1024
	s_waitcnt lgkmcnt(0)
	global_store_dwordx4 v[104:105], v[116:119], off
	ds_read_b64 v[100:101], v150 offset:1024
	ds_read_b64 v[102:103], v151 offset:1024
	s_and_b64 vcc, exec, s[40:41]
	s_cbranch_vccnz .LBB0_1043
	v_pk_mul_f32 v[98:99], v[98:99], v[236:237]
	v_pk_mul_f32 v[96:97], v[96:97], v[234:235]
	v_pk_mul_f32 v[94:95], v[94:95], v[240:241]
	v_pk_mul_f32 v[92:93], v[92:93], v[238:239]
.LBB0_1043:
	s_and_b64 vcc, exec, s[40:41]
	s_cbranch_vccnz .LBB0_1045
	v_pk_mul_f32 v[90:91], v[90:91], v[244:245]
	v_pk_mul_f32 v[88:89], v[88:89], v[242:243]
	v_pk_mul_f32 v[86:87], v[86:87], v[248:249]
	v_pk_mul_f32 v[84:85], v[84:85], v[246:247]
.LBB0_1045:
	v_mov_b32_e32 v106, v3
	v_mov_b32_e32 v107, v3
	v_cvt_pk_fp8_f32 v106, v96, v97
	v_cvt_pk_fp8_f32 v107, v92, v93
	v_mov_b32_e32 v92, v3
	v_mov_b32_e32 v93, v3
	v_cvt_pk_fp8_f32 v92, v88, v89
	v_cvt_pk_fp8_f32 v93, v84, v85
	v_cvt_pk_fp8_f32 v106, v98, v99 op_sel:[0,0,1]
	v_cvt_pk_fp8_f32 v107, v94, v95 op_sel:[0,0,1]
	v_cvt_pk_fp8_f32 v92, v90, v91 op_sel:[0,0,1]
	v_cvt_pk_fp8_f32 v93, v86, v87 op_sel:[0,0,1]
	v_add_co_u32_e32 v84, vcc, 0x4000, v104
	ds_write_b64 v148, v[106:107]
	ds_write_b64 v149, v[92:93]
	v_addc_co_u32_e32 v85, vcc, 0, v105, vcc
	s_waitcnt lgkmcnt(0)
	global_store_dwordx4 v[84:85], v[100:103], off
	ds_read_b64 v[84:85], v150
	ds_read_b64 v[86:87], v151
	s_and_b64 vcc, exec, s[40:41]
	s_cbranch_vccnz .LBB0_1047
	v_pk_mul_f32 v[82:83], v[82:83], v[236:237]
	v_pk_mul_f32 v[80:81], v[80:81], v[234:235]
	v_pk_mul_f32 v[78:79], v[78:79], v[240:241]
	v_pk_mul_f32 v[76:77], v[76:77], v[238:239]
; #define GAS __attribute__((address_space(1)))
; #define LAS __attribute__((address_space(3)))
;     __device__ __forceinline__ void operator()(const f32x4 (&acc)[2][2][4][2], const Unit& u, const float (&rs)[2][4], int wr, int wc, int fr, int fq) const {
;     ...
;         F8_PACKW(0);
; #pragma unroll
;         for (int st = 0; st < 8; ++st) {
;             asm volatile("" ::: "memory");
;             const u32x2_t a = *(const LAS u32x2_t*)(rp0 + (st & 1) * 1024), b = *(const LAS u32x2_t*)(rp1 + (st & 1) * 1024);
;             asm volatile("" ::: "memory");
;             if (st + 1 < 8) F8_PACKW(st + 1);
;             u32x4 o; o.x = a.x; o.y = a.y; o.z = b.x; o.w = b.y;
;             *(GAS u32x4*)(gp + (size_t)((st >> 2) * HALF + (st & 3) * 16) * ldc) = o; }
.LBB0_1047:
	s_and_b64 vcc, exec, s[40:41]
	s_cbranch_vccnz .LBB0_1049
	v_pk_mul_f32 v[74:75], v[74:75], v[244:245]
	v_pk_mul_f32 v[72:73], v[72:73], v[242:243]
	v_pk_mul_f32 v[70:71], v[70:71], v[248:249]
	v_pk_mul_f32 v[68:69], v[68:69], v[246:247]
.LBB0_1049:
	v_mov_b32_e32 v88, v3
	v_mov_b32_e32 v89, v3
	v_cvt_pk_fp8_f32 v88, v80, v81
	v_cvt_pk_fp8_f32 v89, v76, v77
	v_mov_b32_e32 v76, v3
	v_mov_b32_e32 v77, v3
	v_cvt_pk_fp8_f32 v76, v72, v73
	v_cvt_pk_fp8_f32 v77, v68, v69
	v_cvt_pk_fp8_f32 v88, v82, v83 op_sel:[0,0,1]
	v_cvt_pk_fp8_f32 v89, v78, v79 op_sel:[0,0,1]
	v_cvt_pk_fp8_f32 v76, v74, v75 op_sel:[0,0,1]
	v_cvt_pk_fp8_f32 v77, v70, v71 op_sel:[0,0,1]
	v_add_co_u32_e32 v68, vcc, 0x8000, v104
	ds_write_b64 v148, v[88:89] offset:1024
	ds_write_b64 v149, v[76:77] offset:1024
	v_addc_co_u32_e32 v69, vcc, 0, v105, vcc
	s_waitcnt lgkmcnt(0)
	global_store_dwordx4 v[68:69], v[84:87], off
	ds_read_b64 v[68:69], v150 offset:1024
	ds_read_b64 v[70:71], v151 offset:1024
	s_and_b64 vcc, exec, s[40:41]
	s_cbranch_vccnz .LBB0_1051
	v_pk_mul_f32 v[66:67], v[66:67], v[236:237]
	v_pk_mul_f32 v[64:65], v[64:65], v[234:235]
	v_pk_mul_f32 v[62:63], v[62:63], v[240:241]
	v_pk_mul_f32 v[60:61], v[60:61], v[238:239]
.LBB0_1051:
	s_and_b64 vcc, exec, s[40:41]
	s_cbranch_vccnz .LBB0_1053
	v_pk_mul_f32 v[58:59], v[58:59], v[244:245]
	v_pk_mul_f32 v[56:57], v[56:57], v[242:243]
	v_pk_mul_f32 v[54:55], v[54:55], v[248:249]
	v_pk_mul_f32 v[52:53], v[52:53], v[246:247]
.LBB0_1053:
	v_mov_b32_e32 v72, v3
	v_mov_b32_e32 v73, v3
	v_cvt_pk_fp8_f32 v72, v64, v65
	v_cvt_pk_fp8_f32 v73, v60, v61
	v_mov_b32_e32 v60, v3
	v_mov_b32_e32 v61, v3
	v_cvt_pk_fp8_f32 v60, v56, v57
	v_cvt_pk_fp8_f32 v61, v52, v53
	v_cvt_pk_fp8_f32 v72, v66, v67 op_sel:[0,0,1]
	v_cvt_pk_fp8_f32 v73, v62, v63 op_sel:[0,0,1]
	v_cvt_pk_fp8_f32 v60, v58, v59 op_sel:[0,0,1]
	v_cvt_pk_fp8_f32 v61, v54, v55 op_sel:[0,0,1]
	v_add_co_u32_e32 v52, vcc, 0xc000, v104
	ds_write_b64 v148, v[72:73]
	ds_write_b64 v149, v[60:61]
	v_addc_co_u32_e32 v53, vcc, 0, v105, vcc
	s_waitcnt lgkmcnt(0)
	global_store_dwordx4 v[52:53], v[68:71], off
	ds_read_b64 v[52:53], v150
	ds_read_b64 v[54:55], v151
	s_and_b64 vcc, exec, s[40:41]
	s_cbranch_vccnz .LBB0_1055
	v_pk_mul_f32 v[50:51], v[50:51], v[236:237]
	v_pk_mul_f32 v[48:49], v[48:49], v[234:235]
	v_pk_mul_f32 v[46:47], v[46:47], v[240:241]
	v_pk_mul_f32 v[44:45], v[44:45], v[238:239]
.LBB0_1055:
	s_and_b64 vcc, exec, s[40:41]
	s_cbranch_vccnz .LBB0_1057
	v_pk_mul_f32 v[42:43], v[42:43], v[244:245]
	v_pk_mul_f32 v[40:41], v[40:41], v[242:243]
	v_pk_mul_f32 v[38:39], v[38:39], v[248:249]
	v_pk_mul_f32 v[36:37], v[36:37], v[246:247]
.LBB0_1057:
	v_mov_b32_e32 v56, v3
	v_mov_b32_e32 v57, v3
	v_cvt_pk_fp8_f32 v56, v48, v49
	v_cvt_pk_fp8_f32 v57, v44, v45
	v_mov_b32_e32 v44, v3
	v_mov_b32_e32 v45, v3
	v_cvt_pk_fp8_f32 v44, v40, v41
	v_cvt_pk_fp8_f32 v45, v36, v37
	v_cvt_pk_fp8_f32 v56, v50, v51 op_sel:[0,0,1]
	v_cvt_pk_fp8_f32 v57, v46, v47 op_sel:[0,0,1]
	v_cvt_pk_fp8_f32 v44, v42, v43 op_sel:[0,0,1]
	v_cvt_pk_fp8_f32 v45, v38, v39 op_sel:[0,0,1]
	v_add_co_u32_e32 v36, vcc, 0x20000, v104
	ds_write_b64 v148, v[56:57] offset:1024
	ds_write_b64 v149, v[44:45] offset:1024
	v_addc_co_u32_e32 v37, vcc, 0, v105, vcc
	s_waitcnt lgkmcnt(0)
	global_store_dwordx4 v[36:37], v[52:55], off
	ds_read_b64 v[36:37], v150 offset:1024
	ds_read_b64 v[38:39], v151 offset:1024
	s_and_b64 vcc, exec, s[40:41]
	s_cbranch_vccnz .LBB0_1059
	v_pk_mul_f32 v[34:35], v[34:35], v[236:237]
	v_pk_mul_f32 v[32:33], v[32:33], v[234:235]
	v_pk_mul_f32 v[30:31], v[30:31], v[240:241]
	v_pk_mul_f32 v[28:29], v[28:29], v[238:239]
.LBB0_1059:
	s_and_b64 vcc, exec, s[40:41]
	s_cbranch_vccnz .LBB0_1061
	v_pk_mul_f32 v[26:27], v[26:27], v[244:245]
	v_pk_mul_f32 v[24:25], v[24:25], v[242:243]
	v_pk_mul_f32 v[22:23], v[22:23], v[248:249]
	v_pk_mul_f32 v[20:21], v[20:21], v[246:247]
.LBB0_1061:
	v_mov_b32_e32 v40, v3
	v_mov_b32_e32 v41, v3
	v_cvt_pk_fp8_f32 v40, v32, v33
	v_cvt_pk_fp8_f32 v41, v28, v29
	v_mov_b32_e32 v28, v3
	v_mov_b32_e32 v29, v3
	v_cvt_pk_fp8_f32 v28, v24, v25
	v_cvt_pk_fp8_f32 v29, v20, v21
	v_cvt_pk_fp8_f32 v40, v34, v35 op_sel:[0,0,1]
	v_cvt_pk_fp8_f32 v41, v30, v31 op_sel:[0,0,1]
	v_cvt_pk_fp8_f32 v28, v26, v27 op_sel:[0,0,1]
	v_cvt_pk_fp8_f32 v29, v22, v23 op_sel:[0,0,1]
	v_add_co_u32_e32 v20, vcc, 0x24000, v104
	ds_write_b64 v148, v[40:41]
	ds_write_b64 v149, v[28:29]
	v_addc_co_u32_e32 v21, vcc, 0, v105, vcc
	s_waitcnt lgkmcnt(0)
	global_store_dwordx4 v[20:21], v[36:39], off
	ds_read_b64 v[20:21], v150
	ds_read_b64 v[22:23], v151
	s_and_b64 vcc, exec, s[40:41]
	s_cbranch_vccnz .LBB0_1063
	v_pk_mul_f32 v[18:19], v[18:19], v[236:237]
	v_pk_mul_f32 v[16:17], v[16:17], v[234:235]
	v_pk_mul_f32 v[14:15], v[14:15], v[240:241]
	v_pk_mul_f32 v[12:13], v[12:13], v[238:239]
.LBB0_1063:
	s_and_b64 vcc, exec, s[40:41]
	s_cbranch_vccnz .LBB0_1065
	v_pk_mul_f32 v[10:11], v[10:11], v[244:245]
	v_pk_mul_f32 v[8:9], v[8:9], v[242:243]
	v_pk_mul_f32 v[6:7], v[6:7], v[248:249]
	v_pk_mul_f32 v[4:5], v[4:5], v[246:247]
